# mLSTM output unit: wave-uniform branch tests with a fixed outcome (tid < 512) folded in the epilogue gather/store chains
# speedup vs baseline: 1.0008x; 1.0008x over previous
; template <bool OUT, bool PASS2>
; __device__ __forceinline__ void ml_block(const Args& a, unsigned char* lds_g, int rowbase, int h, int dir, f32x4 (&st)[9], int tid) {
;     ...
;     if (OUT) {
; #pragma unroll
;         for (int x = 0; x < 5; ++x) { const int vt = vh * 5 + x; hgv[x] = vt < 8 ? a.in[I_HEADG][h * 128 + 16 * vt + fr] : 0.f; } }
.LBB0_387:
	s_add_i32 s34, s35, 2
	v_mov_b32_e32 v187, 0
	s_and_b64 vcc, exec, s[22:23]
	v_mov_b32_e32 v188, 0
	v_lshl_add_u32 v4, s34, 4, v178
	v_lshl_add_u64 v[0:1], v[4:5], 2, s[58:59]
	global_load_dword v188, v[0:1], off

; template <bool OUT, bool PASS2>
; __device__ __forceinline__ void ml_block(const Args& a, unsigned char* lds_g, int rowbase, int h, int dir, f32x4 (&st)[9], int tid) {
;     ...
;             for (int r = 0; r < 4; ++r) { const size_t ob = (size_t)(rowbase - NCTX + 64 * c + 16 * ti + 4 * fq + r) * 1024 + h * 128;
; #pragma unroll
;                 for (int x = 0; x < 5; ++x) { const int vt = vh * 5 + x; if (vt < 8) { ogv[x][r] = OGp[ob + 16 * vt + fr]; if (PASS2) tmv[x][r] = TMp[ob + 16 * vt + fr]; } } }
.LBB0_395:
	v_add_u32_e32 v6, s73, v205
	v_ashrrev_i32_e32 v7, 31, v6
	v_lshlrev_b64 v[128:129], 11, v[6:7]
	v_lshl_add_u64 v[68:69], v[138:139], 0, v[128:129]
	s_branch .LBB0_426
	s_branch .LBB0_427

; template <bool OUT, bool PASS2>
; __device__ __forceinline__ void ml_block(const Args& a, unsigned char* lds_g, int rowbase, int h, int dir, f32x4 (&st)[9], int tid) {
;     ...
;             for (int r = 0; r < 4; ++r) { const size_t ob = (size_t)(rowbase - NCTX + 64 * c + 16 * ti + 4 * fq + r) * 1024 + h * 128;
; #pragma unroll
;                 for (int x = 0; x < 5; ++x) { const int vt = vh * 5 + x; if (vt < 8) { ogv[x][r] = OGp[ob + 16 * vt + fr]; if (PASS2) tmv[x][r] = TMp[ob + 16 * vt + fr]; } } }
.LBB0_401:
	v_add_u32_e32 v68, 1, v6
	v_ashrrev_i32_e32 v69, 31, v68
	v_lshlrev_b64 v[144:145], 11, v[68:69]
	v_lshl_add_u64 v[68:69], v[138:139], 0, v[144:145]
	s_branch .LBB0_430
	s_branch .LBB0_431

; template <bool OUT, bool PASS2>
; __device__ __forceinline__ void ml_block(const Args& a, unsigned char* lds_g, int rowbase, int h, int dir, f32x4 (&st)[9], int tid) {
;     ...
;             for (int r = 0; r < 4; ++r) { const size_t ob = (size_t)(rowbase - NCTX + 64 * c + 16 * ti + 4 * fq + r) * 1024 + h * 128;
; #pragma unroll
;                 for (int x = 0; x < 5; ++x) { const int vt = vh * 5 + x; if (vt < 8) { ogv[x][r] = OGp[ob + 16 * vt + fr]; if (PASS2) tmv[x][r] = TMp[ob + 16 * vt + fr]; } } }
.LBB0_407:
	v_add_u32_e32 v68, 2, v6
	v_ashrrev_i32_e32 v69, 31, v68
	v_lshlrev_b64 v[140:141], 11, v[68:69]
	v_lshl_add_u64 v[68:69], v[138:139], 0, v[140:141]
	s_branch .LBB0_434
	s_branch .LBB0_435

; template <bool OUT, bool PASS2>
; __device__ __forceinline__ void ml_block(const Args& a, unsigned char* lds_g, int rowbase, int h, int dir, f32x4 (&st)[9], int tid) {
;     ...
;             for (int r = 0; r < 4; ++r) { const size_t ob = (size_t)(rowbase - NCTX + 64 * c + 16 * ti + 4 * fq + r) * 1024 + h * 128;
; #pragma unroll
;                 for (int x = 0; x < 5; ++x) { const int vt = vh * 5 + x; if (vt < 8) { ogv[x][r] = OGp[ob + 16 * vt + fr]; if (PASS2) tmv[x][r] = TMp[ob + 16 * vt + fr]; } } }
.LBB0_413:
	v_add_u32_e32 v6, 3, v6
	v_ashrrev_i32_e32 v7, 31, v6
	v_lshlrev_b64 v[142:143], 11, v[6:7]
	v_lshl_add_u64 v[6:7], v[138:139], 0, v[142:143]
	s_branch .LBB0_438
	s_branch .LBB0_439

; template <bool OUT, bool PASS2>
; __device__ __forceinline__ void ml_block(const Args& a, unsigned char* lds_g, int rowbase, int h, int dir, f32x4 (&st)[9], int tid) {
;     ...
;             for (int r = 0; r < 4; ++r) { const size_t ob = (size_t)(rowbase - NCTX + 64 * c + 16 * ti + 4 * fq + r) * 1024 + h * 128;
; #pragma unroll
;                 for (int x = 0; x < 5; ++x) { const int vt = vh * 5 + x; if (vt < 8) { ogv[x][r] = OGp[ob + 16 * vt + fr]; if (PASS2) tmv[x][r] = TMp[ob + 16 * vt + fr]; } } }
.LBB0_426:
	s_lshl_b32 s60, s33, 1
	v_lshl_add_u64 v[70:71], v[68:69], 0, s[60:61]
	global_load_ushort v211, v[70:71], off
.LBB0_427:
	s_lshl_b32 s60, s43, 1
	v_lshl_add_u64 v[70:71], v[68:69], 0, s[60:61]
	global_load_ushort v215, v[70:71], off
.LBB0_428:
	s_lshl_b32 s60, s48, 1
	v_lshl_add_u64 v[70:71], v[68:69], 0, s[60:61]
	global_load_ushort v219, v[70:71], off
	s_and_b64 vcc, exec, s[26:27]
	s_cbranch_vccnz .LBB0_399

; template <bool OUT, bool PASS2>
; __device__ __forceinline__ void ml_block(const Args& a, unsigned char* lds_g, int rowbase, int h, int dir, f32x4 (&st)[9], int tid) {
;     ...
;             for (int r = 0; r < 4; ++r) { const size_t ob = (size_t)(rowbase - NCTX + 64 * c + 16 * ti + 4 * fq + r) * 1024 + h * 128;
; #pragma unroll
;                 for (int x = 0; x < 5; ++x) { const int vt = vh * 5 + x; if (vt < 8) { ogv[x][r] = OGp[ob + 16 * vt + fr]; if (PASS2) tmv[x][r] = TMp[ob + 16 * vt + fr]; } } }
.LBB0_430:
	s_lshl_b32 s60, s33, 1
	v_lshl_add_u64 v[70:71], v[68:69], 0, s[60:61]
	global_load_ushort v212, v[70:71], off
.LBB0_431:
	s_lshl_b32 s60, s43, 1
	v_lshl_add_u64 v[70:71], v[68:69], 0, s[60:61]
	global_load_ushort v216, v[70:71], off
.LBB0_432:
	s_lshl_b32 s60, s48, 1
	v_lshl_add_u64 v[70:71], v[68:69], 0, s[60:61]
	global_load_ushort v221, v[70:71], off
	s_and_b64 vcc, exec, s[26:27]
	s_cbranch_vccnz .LBB0_405

; template <bool OUT, bool PASS2>
; __device__ __forceinline__ void ml_block(const Args& a, unsigned char* lds_g, int rowbase, int h, int dir, f32x4 (&st)[9], int tid) {
;     ...
;             for (int r = 0; r < 4; ++r) { const size_t ob = (size_t)(rowbase - NCTX + 64 * c + 16 * ti + 4 * fq + r) * 1024 + h * 128;
; #pragma unroll
;                 for (int x = 0; x < 5; ++x) { const int vt = vh * 5 + x; if (vt < 8) { ogv[x][r] = OGp[ob + 16 * vt + fr]; if (PASS2) tmv[x][r] = TMp[ob + 16 * vt + fr]; } } }
.LBB0_434:
	s_lshl_b32 s60, s33, 1
	v_lshl_add_u64 v[70:71], v[68:69], 0, s[60:61]
	global_load_ushort v213, v[70:71], off
.LBB0_435:
	s_lshl_b32 s60, s43, 1
	v_lshl_add_u64 v[70:71], v[68:69], 0, s[60:61]
	global_load_ushort v217, v[70:71], off
.LBB0_436:
	s_lshl_b32 s60, s48, 1
	v_lshl_add_u64 v[70:71], v[68:69], 0, s[60:61]
	global_load_ushort v223, v[70:71], off
	s_and_b64 vcc, exec, s[26:27]
	s_cbranch_vccnz .LBB0_411

; template <bool OUT, bool PASS2>
; __device__ __forceinline__ void ml_block(const Args& a, unsigned char* lds_g, int rowbase, int h, int dir, f32x4 (&st)[9], int tid) {
;     ...
;             for (int r = 0; r < 4; ++r) { const size_t ob = (size_t)(rowbase - NCTX + 64 * c + 16 * ti + 4 * fq + r) * 1024 + h * 128;
; #pragma unroll
;                 for (int x = 0; x < 5; ++x) { const int vt = vh * 5 + x; if (vt < 8) { ogv[x][r] = OGp[ob + 16 * vt + fr]; if (PASS2) tmv[x][r] = TMp[ob + 16 * vt + fr]; } } }
.LBB0_438:
	s_lshl_b32 s60, s33, 1
	v_lshl_add_u64 v[68:69], v[6:7], 0, s[60:61]
	global_load_ushort v214, v[68:69], off
.LBB0_439:
	s_lshl_b32 s60, s43, 1
	v_lshl_add_u64 v[68:69], v[6:7], 0, s[60:61]
	global_load_ushort v218, v[68:69], off
.LBB0_440:
	s_lshl_b32 s60, s48, 1
	v_lshl_add_u64 v[68:69], v[6:7], 0, s[60:61]
	global_load_ushort v225, v[68:69], off
	s_and_b64 vcc, exec, s[26:27]
	s_cbranch_vccnz .LBB0_417

; template <bool OUT, bool PASS2>
; __device__ __forceinline__ void ml_block(const Args& a, unsigned char* lds_g, int rowbase, int h, int dir, f32x4 (&st)[9], int tid) {
;     ...
;     if (OUT) {
; #pragma unroll
;         for (int x = 0; x < 5; ++x) { const int vt = vh * 5 + x; hgv[x] = vt < 8 ? a.in[I_HEADG][h * 128 + 16 * vt + fr] : 0.f; } }
.LBB0_529:
	s_add_i32 s30, s33, 2
	v_mov_b32_e32 v184, 0
	s_and_b64 vcc, exec, s[22:23]
	v_mov_b32_e32 v185, 0
	v_lshl_add_u32 v4, s30, 4, v178
	v_lshl_add_u64 v[0:1], v[4:5], 2, s[58:59]
	global_load_dword v185, v[0:1], off

; template <bool OUT, bool PASS2>
; __device__ __forceinline__ void ml_block(const Args& a, unsigned char* lds_g, int rowbase, int h, int dir, f32x4 (&st)[9], int tid) {
;     ...
;             for (int r = 0; r < 4; ++r) { const size_t ob = (size_t)(rowbase - NCTX + 64 * c + 16 * ti + 4 * fq + r) * 1024 + h * 128;
; #pragma unroll
;                 for (int x = 0; x < 5; ++x) { const int vt = vh * 5 + x; if (vt < 8) { ogv[x][r] = OGp[ob + 16 * vt + fr]; if (PASS2) tmv[x][r] = TMp[ob + 16 * vt + fr]; } } }
.LBB0_537:
	v_add_u32_e32 v2, s64, v202
	v_add_u32_e32 v136, 0xc0, v2
	v_ashrrev_i32_e32 v137, 31, v136
	v_lshlrev_b64 v[0:1], 10, v[136:137]
	v_or_b32_e32 v0, v0, v178
	s_branch .LBB0_628
	s_branch .LBB0_629

; template <bool OUT, bool PASS2>
; __device__ __forceinline__ void ml_block(const Args& a, unsigned char* lds_g, int rowbase, int h, int dir, f32x4 (&st)[9], int tid) {
;     ...
;             for (int r = 0; r < 4; ++r) { const size_t ob = (size_t)(rowbase - NCTX + 64 * c + 16 * ti + 4 * fq + r) * 1024 + h * 128;
; #pragma unroll
;                 for (int x = 0; x < 5; ++x) { const int vt = vh * 5 + x; if (vt < 8) { ogv[x][r] = OGp[ob + 16 * vt + fr]; if (PASS2) tmv[x][r] = TMp[ob + 16 * vt + fr]; } } }
.LBB0_543:
	v_add_u32_e32 v138, 0xc1, v2
	v_ashrrev_i32_e32 v139, 31, v138
	v_lshlrev_b64 v[0:1], 10, v[138:139]
	v_or_b32_e32 v0, v0, v178
	s_branch .LBB0_632
	s_branch .LBB0_633

; template <bool OUT, bool PASS2>
; __device__ __forceinline__ void ml_block(const Args& a, unsigned char* lds_g, int rowbase, int h, int dir, f32x4 (&st)[9], int tid) {
;     ...
;             for (int r = 0; r < 4; ++r) { const size_t ob = (size_t)(rowbase - NCTX + 64 * c + 16 * ti + 4 * fq + r) * 1024 + h * 128;
; #pragma unroll
;                 for (int x = 0; x < 5; ++x) { const int vt = vh * 5 + x; if (vt < 8) { ogv[x][r] = OGp[ob + 16 * vt + fr]; if (PASS2) tmv[x][r] = TMp[ob + 16 * vt + fr]; } } }
.LBB0_549:
	v_add_u32_e32 v140, 0xc2, v2
	v_ashrrev_i32_e32 v141, 31, v140
	v_lshlrev_b64 v[0:1], 10, v[140:141]
	v_or_b32_e32 v0, v0, v178
	s_branch .LBB0_636
	s_branch .LBB0_637

; template <bool OUT, bool PASS2>
; __device__ __forceinline__ void ml_block(const Args& a, unsigned char* lds_g, int rowbase, int h, int dir, f32x4 (&st)[9], int tid) {
;     ...
;             for (int r = 0; r < 4; ++r) { const size_t ob = (size_t)(rowbase - NCTX + 64 * c + 16 * ti + 4 * fq + r) * 1024 + h * 128;
; #pragma unroll
;                 for (int x = 0; x < 5; ++x) { const int vt = vh * 5 + x; if (vt < 8) { ogv[x][r] = OGp[ob + 16 * vt + fr]; if (PASS2) tmv[x][r] = TMp[ob + 16 * vt + fr]; } } }
.LBB0_555:
	v_add_u32_e32 v142, 0xc3, v2
	v_ashrrev_i32_e32 v143, 31, v142
	v_lshlrev_b64 v[0:1], 10, v[142:143]
	v_or_b32_e32 v0, v0, v178
	s_branch .LBB0_640
	s_branch .LBB0_641

; template <bool OUT, bool PASS2>
; __device__ __forceinline__ void ml_block(const Args& a, unsigned char* lds_g, int rowbase, int h, int dir, f32x4 (&st)[9], int tid) {
;     ...
;             for (int r = 0; r < 4; ++r) { const size_t ob = (size_t)(rowbase - NCTX + 64 * c + 16 * ti + 4 * fq + r) * 1024 + h * 128;
; #pragma unroll
;                 for (int x = 0; x < 5; ++x) { const int vt = vh * 5 + x; if (vt < 8) { ogv[x][r] = OGp[ob + 16 * vt + fr]; if (PASS2) tmv[x][r] = TMp[ob + 16 * vt + fr]; } } }
.LBB0_628:
	v_or_b32_e32 v6, s44, v0
	v_mov_b32_e32 v7, v1
	v_lshlrev_b64 v[6:7], 1, v[6:7]
	v_lshl_add_u64 v[72:73], s[56:57], 0, v[6:7]
	v_lshl_add_u64 v[6:7], s[54:55], 0, v[6:7]
	global_load_ushort v229, v[72:73], off
	global_load_ushort v209, v[6:7], off
.LBB0_629:
	v_or_b32_e32 v6, s45, v0
	v_mov_b32_e32 v7, v1
	v_lshlrev_b64 v[6:7], 1, v[6:7]
	v_lshl_add_u64 v[72:73], s[56:57], 0, v[6:7]
	v_lshl_add_u64 v[6:7], s[54:55], 0, v[6:7]
	global_load_ushort v233, v[72:73], off
	global_load_ushort v213, v[6:7], off
.LBB0_630:
	v_or_b32_e32 v6, s60, v0
	v_mov_b32_e32 v7, v1
	v_lshlrev_b64 v[6:7], 1, v[6:7]
	v_lshl_add_u64 v[72:73], s[56:57], 0, v[6:7]
	v_lshl_add_u64 v[6:7], s[54:55], 0, v[6:7]
	global_load_ushort v237, v[72:73], off
	global_load_ushort v217, v[6:7], off
	s_and_b64 vcc, exec, s[26:27]
	v_lshlrev_b64 v[0:1], 1, v[0:1]
	s_cbranch_vccnz .LBB0_541

; template <bool OUT, bool PASS2>
; __device__ __forceinline__ void ml_block(const Args& a, unsigned char* lds_g, int rowbase, int h, int dir, f32x4 (&st)[9], int tid) {
;     ...
;             for (int r = 0; r < 4; ++r) { const size_t ob = (size_t)(rowbase - NCTX + 64 * c + 16 * ti + 4 * fq + r) * 1024 + h * 128;
; #pragma unroll
;                 for (int x = 0; x < 5; ++x) { const int vt = vh * 5 + x; if (vt < 8) { ogv[x][r] = OGp[ob + 16 * vt + fr]; if (PASS2) tmv[x][r] = TMp[ob + 16 * vt + fr]; } } }
.LBB0_632:
	v_or_b32_e32 v6, s44, v0
	v_mov_b32_e32 v7, v1
	v_lshlrev_b64 v[6:7], 1, v[6:7]
	v_lshl_add_u64 v[72:73], s[56:57], 0, v[6:7]
	v_lshl_add_u64 v[6:7], s[54:55], 0, v[6:7]
	global_load_ushort v230, v[72:73], off
	global_load_ushort v210, v[6:7], off
.LBB0_633:
	v_or_b32_e32 v6, s45, v0
	v_mov_b32_e32 v7, v1
	v_lshlrev_b64 v[6:7], 1, v[6:7]
	v_lshl_add_u64 v[72:73], s[56:57], 0, v[6:7]
	v_lshl_add_u64 v[6:7], s[54:55], 0, v[6:7]
	global_load_ushort v234, v[72:73], off
	global_load_ushort v214, v[6:7], off
.LBB0_634:
	v_or_b32_e32 v6, s60, v0
	v_mov_b32_e32 v7, v1
	v_lshlrev_b64 v[6:7], 1, v[6:7]
	v_lshl_add_u64 v[72:73], s[56:57], 0, v[6:7]
	v_lshl_add_u64 v[6:7], s[54:55], 0, v[6:7]
	global_load_ushort v238, v[72:73], off
	global_load_ushort v218, v[6:7], off
	s_and_b64 vcc, exec, s[26:27]
	v_lshlrev_b64 v[0:1], 1, v[0:1]
	s_cbranch_vccnz .LBB0_547

; template <bool OUT, bool PASS2>
; __device__ __forceinline__ void ml_block(const Args& a, unsigned char* lds_g, int rowbase, int h, int dir, f32x4 (&st)[9], int tid) {
;     ...
;             for (int r = 0; r < 4; ++r) { const size_t ob = (size_t)(rowbase - NCTX + 64 * c + 16 * ti + 4 * fq + r) * 1024 + h * 128;
; #pragma unroll
;                 for (int x = 0; x < 5; ++x) { const int vt = vh * 5 + x; if (vt < 8) { ogv[x][r] = OGp[ob + 16 * vt + fr]; if (PASS2) tmv[x][r] = TMp[ob + 16 * vt + fr]; } } }
.LBB0_636:
	v_or_b32_e32 v6, s44, v0
	v_mov_b32_e32 v7, v1
	v_lshlrev_b64 v[6:7], 1, v[6:7]
	v_lshl_add_u64 v[72:73], s[56:57], 0, v[6:7]
	v_lshl_add_u64 v[6:7], s[54:55], 0, v[6:7]
	global_load_ushort v231, v[72:73], off
	global_load_ushort v211, v[6:7], off
.LBB0_637:
	v_or_b32_e32 v6, s45, v0
	v_mov_b32_e32 v7, v1
	v_lshlrev_b64 v[6:7], 1, v[6:7]
	v_lshl_add_u64 v[72:73], s[56:57], 0, v[6:7]
	v_lshl_add_u64 v[6:7], s[54:55], 0, v[6:7]
	global_load_ushort v235, v[72:73], off
	global_load_ushort v215, v[6:7], off
.LBB0_638:
	v_or_b32_e32 v6, s60, v0
	v_mov_b32_e32 v7, v1
	v_lshlrev_b64 v[6:7], 1, v[6:7]
	v_lshl_add_u64 v[72:73], s[56:57], 0, v[6:7]
	v_lshl_add_u64 v[6:7], s[54:55], 0, v[6:7]
	global_load_ushort v240, v[72:73], off
	global_load_ushort v220, v[6:7], off
	s_and_b64 vcc, exec, s[26:27]
	v_lshlrev_b64 v[0:1], 1, v[0:1]
	s_cbranch_vccnz .LBB0_553

; template <bool OUT, bool PASS2>
; __device__ __forceinline__ void ml_block(const Args& a, unsigned char* lds_g, int rowbase, int h, int dir, f32x4 (&st)[9], int tid) {
;     ...
;             for (int r = 0; r < 4; ++r) { const size_t ob = (size_t)(rowbase - NCTX + 64 * c + 16 * ti + 4 * fq + r) * 1024 + h * 128;
; #pragma unroll
;                 for (int x = 0; x < 5; ++x) { const int vt = vh * 5 + x; if (vt < 8) { ogv[x][r] = OGp[ob + 16 * vt + fr]; if (PASS2) tmv[x][r] = TMp[ob + 16 * vt + fr]; } } }
.LBB0_640:
	v_or_b32_e32 v2, s44, v0
	v_mov_b32_e32 v3, v1
	v_lshlrev_b64 v[2:3], 1, v[2:3]
	v_lshl_add_u64 v[6:7], s[56:57], 0, v[2:3]
	v_lshl_add_u64 v[2:3], s[54:55], 0, v[2:3]
	global_load_ushort v232, v[6:7], off
	global_load_ushort v212, v[2:3], off
.LBB0_641:
	v_or_b32_e32 v2, s45, v0
	v_mov_b32_e32 v3, v1
	v_lshlrev_b64 v[2:3], 1, v[2:3]
	v_lshl_add_u64 v[6:7], s[56:57], 0, v[2:3]
	v_lshl_add_u64 v[2:3], s[54:55], 0, v[2:3]
	global_load_ushort v236, v[6:7], off
	global_load_ushort v216, v[2:3], off
.LBB0_642:
	v_or_b32_e32 v2, s60, v0
	v_mov_b32_e32 v3, v1
	v_lshlrev_b64 v[2:3], 1, v[2:3]
	v_lshl_add_u64 v[6:7], s[56:57], 0, v[2:3]
	v_lshl_add_u64 v[2:3], s[54:55], 0, v[2:3]
	global_load_ushort v242, v[6:7], off
	global_load_ushort v222, v[2:3], off
	s_and_b64 vcc, exec, s[26:27]
	v_lshlrev_b64 v[0:1], 1, v[0:1]
	s_cbranch_vccnz .LBB0_559
